# GB phase: deferred weight conversion on 2 of the 8 waves per converting workgroup (fewer loads in flight beside the latency-bound DeltaNet chain)
# speedup vs baseline: 1.0105x; 1.0105x over previous
.LBB0_1704:
	s_and_b64 vcc, exec, s[0:1]
	s_cbranch_vccz .LBB0_1766
	s_cmpk_lt_i32 s16, 0x80
	s_cbranch_scc1 .LBB0_1766
	s_cmp_gt_u32 s18, 1
	s_cbranch_scc1 .LBB0_1766
	s_mul_i32 s1, s18, 0x2200
	v_lshrrev_b32_e32 v106, 3, v1
	v_lshlrev_b32_e32 v0, 2, v1
	v_lshlrev_b32_e32 v1, 3, v1
	s_lshl_b32 s0, s16, 1
	s_add_i32 s1, s1, 0
	v_and_b32_e32 v0, 28, v0
	v_and_b32_e32 v2, 56, v1
	s_add_i32 s0, s0, s18
	v_readlane_b32 s2, v254, 62
	s_waitcnt vmcnt(0)
	v_mul_u32_u24_e32 v4, 0x84, v2
	v_lshl_add_u32 v5, v0, 2, s1
	v_mul_u32_u24_e32 v6, 0x84, v106
	v_lshlrev_b32_e32 v7, 2, v106
	v_mov_b32_e32 v68, 0
	s_add_i32 s16, s2, s0
	v_or_b32_e32 v1, 8, v106
	v_or_b32_e32 v107, 16, v106
	v_or_b32_e32 v108, 24, v106
	v_add3_u32 v109, s1, v4, v7
	s_mov_b32 s18, 0
	v_lshlrev_b32_e32 v100, 1, v2
	v_add_u32_e32 v110, v5, v6
	s_mov_b32 s19, 0
	v_mov_b32_e32 v69, v68
	v_mov_b32_e32 v70, v68
	v_mov_b32_e32 v71, v68
	v_mov_b32_e32 v72, v68
	v_mov_b32_e32 v73, v68
	v_mov_b32_e32 v74, v68
	v_mov_b32_e32 v75, v68
	v_mov_b32_e32 v76, v68
	v_mov_b32_e32 v77, v68
	v_mov_b32_e32 v78, v68
	v_mov_b32_e32 v79, v68
	v_mov_b32_e32 v80, v68
	v_mov_b32_e32 v81, v68
	v_mov_b32_e32 v82, v68
	v_mov_b32_e32 v83, v68
	v_mov_b32_e32 v84, v68
	v_mov_b32_e32 v85, v68
	v_mov_b32_e32 v86, v68
	v_mov_b32_e32 v87, v68
	v_mov_b32_e32 v88, v68
	v_mov_b32_e32 v89, v68
	v_mov_b32_e32 v90, v68
	v_mov_b32_e32 v91, v68
	v_mov_b32_e32 v92, v68
	v_mov_b32_e32 v93, v68
	v_mov_b32_e32 v94, v68
	v_mov_b32_e32 v95, v68
	v_mov_b32_e32 v96, v68
	v_mov_b32_e32 v97, v68
	v_mov_b32_e32 v98, v68
	v_mov_b32_e32 v99, v68
	s_branch .LBB0_1710

.LBB0_1739:
	s_abs_i32 s9, s18
	v_readlane_b32 s14, v255, 5
	s_lshl_b32 s14, s14, 2
	s_mul_hi_u32 s10, s9, s14
	v_readlane_b32 s11, v255, 4
	s_lshr_b32 s11, s11, 2
	s_mul_i32 s10, s10, s11
	s_lshr_b32 s8, s22, 6
	s_lshr_b32 s25, s20, 5
	s_sub_i32 s9, s9, s10
	s_mul_i32 s23, s25, s8
	s_ashr_i32 s8, s18, 31
	s_sub_i32 s10, s9, s11
	s_cmp_ge_u32 s9, s11
	s_cselect_b32 s9, s10, s9
	s_sub_i32 s10, s9, s11
	s_cmp_ge_u32 s9, s11
	s_cselect_b32 s9, s10, s9
	s_xor_b32 s9, s9, s8
	s_sub_i32 s8, s8, s9
	s_add_i32 s8, s16, s8
	s_ashr_i32 s9, s8, 31
	s_abs_i32 s8, s8
	s_mul_hi_u32 s10, s8, s14
	s_mul_i32 s10, s10, s11
	s_sub_i32 s8, s8, s10
	s_sub_i32 s10, s8, s11
	s_cmp_ge_u32 s8, s11
	s_cselect_b32 s8, s10, s8
	v_cvt_f32_u32_e32 v2, s25
	s_sub_i32 s10, s8, s11
	s_cmp_ge_u32 s8, s11
	s_cselect_b32 s8, s10, s8
	s_xor_b32 s8, s8, s9
	v_rcp_iflag_f32_e32 v101, v2
	s_sub_i32 s26, s8, s9
	s_cmp_lt_i32 s26, s23
	v_cndmask_b32_e64 v2, 0, 1, s[12:13]
	s_mov_b32 s27, 0
	s_cselect_b64 s[10:11], -1, 0
	s_cmp_ge_i32 s26, s23
	v_cmp_ne_u32_e64 s[38:39], 1, v2
	s_mov_b32 s8, 0
	s_cbranch_scc1 .LBB0_1746
	v_mul_f32_e32 v2, 0x4f7ffffe, v101
	v_cvt_u32_f32_e32 v2, v2
	s_sub_i32 s12, 0, s25
	s_abs_i32 s9, s26
	s_ashr_i32 s8, s26, 31
	v_readfirstlane_b32 s13, v2
	s_mul_i32 s12, s12, s13
	s_mul_hi_u32 s12, s13, s12
	s_add_i32 s13, s13, s12
	s_mul_hi_u32 s12, s9, s13
	s_mul_i32 s13, s12, s25
	s_sub_i32 s9, s9, s13
	s_add_i32 s13, s12, 1
	s_sub_i32 s14, s9, s25
	s_cmp_ge_u32 s9, s25
	s_cselect_b32 s12, s13, s12
	s_cselect_b32 s9, s14, s9
	s_add_i32 s13, s12, 1
	s_cmp_ge_u32 s9, s25
	s_cselect_b32 s9, s13, s12
	s_xor_b32 s9, s9, s8
	s_sub_i32 s13, s9, s8
	s_mul_i32 s8, s13, s25
	s_sub_i32 s8, s26, s8
	s_lshl_b32 s12, s8, 5
	s_and_b64 vcc, exec, s[38:39]
	s_mov_b32 s27, s12
	s_cbranch_vccnz .LBB0_1745
	s_cmp_ge_i32 s12, s21
	s_mov_b64 s[8:9], -1
	s_cbranch_scc0 .LBB0_1743
	s_sub_i32 s8, s12, s21
	s_lshl_b32 s8, s8, 1
	s_and_b32 s8, s8, 0x7fffff00
	s_and_b32 s9, s12, 0x60
	s_or_b32 s8, s9, s8
	s_or_b32 s27, s8, 0x80
	s_mov_b64 s[8:9], 0

.LBB0_1746:
	v_readlane_b32 s9, v255, 1
	s_lshr_b32 s9, s9, 2
	s_add_i32 s12, s26, s9
	s_mov_b32 s31, 0
	s_cmp_ge_i32 s12, s23
	s_mov_b32 s14, 0
	s_cbranch_scc1 .LBB0_1753
	v_mul_f32_e32 v2, 0x4f7ffffe, v101
	v_cvt_u32_f32_e32 v2, v2
	s_sub_i32 s14, 0, s25
	s_abs_i32 s13, s12
	s_ashr_i32 s9, s12, 31
	v_readfirstlane_b32 s15, v2
	s_mul_i32 s14, s14, s15
	s_mul_hi_u32 s14, s15, s14
	s_add_i32 s15, s15, s14
	s_mul_hi_u32 s14, s13, s15
	s_mul_i32 s15, s14, s25
	s_sub_i32 s13, s13, s15
	s_add_i32 s15, s14, 1
	s_sub_i32 s31, s13, s25
	s_cmp_ge_u32 s13, s25
	s_cselect_b32 s14, s15, s14
	s_cselect_b32 s13, s31, s13
	s_add_i32 s15, s14, 1
	s_cmp_ge_u32 s13, s25
	s_cselect_b32 s13, s15, s14
	s_xor_b32 s13, s13, s9
	s_sub_i32 s9, s13, s9
	s_mul_i32 s13, s9, s25
	s_sub_i32 s12, s12, s13
	s_lshl_b32 s12, s12, 5
	s_and_b64 vcc, exec, s[38:39]
	s_mov_b32 s31, s12
	s_cbranch_vccnz .LBB0_1752
	s_cmp_ge_i32 s12, s21
	s_mov_b64 s[14:15], -1
	s_cbranch_scc0 .LBB0_1750
	s_sub_i32 s13, s12, s21
	s_lshl_b32 s13, s13, 1
	s_and_b32 s13, s13, 0x7fffff00
	s_and_b32 s14, s12, 0x60
	s_or_b32 s13, s14, s13
	s_or_b32 s31, s13, 0x80
	s_mov_b64 s[14:15], 0

.LBB0_1755:
	v_readlane_b32 s0, v254, 61
	s_lshr_b32 s0, s0, 2
	s_add_i32 s0, s0, s26
	s_mov_b32 s11, s14
	s_mov_b32 s12, s31
	s_mov_b32 s31, 0
	s_cmp_ge_i32 s0, s23
	s_mov_b32 s14, 0
	s_cbranch_scc1 .LBB0_1762
	s_abs_i32 s2, s0
	s_mul_hi_u32 s3, s2, s10
	s_mul_i32 s9, s3, s25
	s_sub_i32 s2, s2, s9
	s_ashr_i32 s1, s0, 31
	s_add_i32 s9, s3, 1
	s_sub_i32 s13, s2, s25
	s_cmp_ge_u32 s2, s25
	s_cselect_b32 s3, s9, s3
	s_cselect_b32 s2, s13, s2
	s_add_i32 s9, s3, 1
	s_cmp_ge_u32 s2, s25
	s_cselect_b32 s2, s9, s3
	s_xor_b32 s2, s2, s1
	s_sub_i32 s1, s2, s1
	s_mul_i32 s2, s1, s25
	s_sub_i32 s9, s0, s2
	s_lshl_b32 s0, s9, 5
	s_and_b64 vcc, exec, s[38:39]
	s_mov_b32 s31, s0
	s_cbranch_vccnz .LBB0_1761
	s_cmp_ge_i32 s0, s21
	s_mov_b64 s[2:3], -1
	s_cbranch_scc0 .LBB0_1759
	s_sub_i32 s2, s0, s21
	s_lshl_b32 s2, s2, 1
	s_and_b32 s2, s2, 0x7fffff00
	s_and_b32 s3, s0, 0x60
	s_or_b32 s2, s3, s2
	s_or_b32 s31, s2, 0x80
	s_mov_b64 s[2:3], 0

.LBB0_1762:
	v_add_u32_e32 v2, 0x8000, v110
	s_waitcnt vmcnt(7)
	ds_write2_b32 v2, v68, v69 offset1:1
	v_add_u32_e32 v2, 0x8008, v110
	ds_write2_b32 v2, v70, v71 offset1:1
	v_add_u32_e32 v2, 0x8420, v110
	s_waitcnt vmcnt(6)
	ds_write2_b32 v2, v72, v73 offset1:1
	v_add_u32_e32 v2, 0x8428, v110
	ds_write2_b32 v2, v74, v75 offset1:1
	v_add_u32_e32 v2, 0x8840, v110
	s_waitcnt vmcnt(5)
	ds_write2_b32 v2, v76, v77 offset1:1
	v_add_u32_e32 v2, 0x8848, v110
	ds_write2_b32 v2, v78, v79 offset1:1
	v_add_u32_e32 v2, 0x8c60, v110
	s_waitcnt vmcnt(4)
	ds_write2_b32 v2, v80, v81 offset1:1
	v_add_u32_e32 v2, 0x8c68, v110
	ds_write2_b32 v2, v82, v83 offset1:1
	v_add_u32_e32 v2, 0x9080, v110
	s_waitcnt vmcnt(3)
	ds_write2_b32 v2, v84, v85 offset1:1
	v_add_u32_e32 v2, 0x9088, v110
	ds_write2_b32 v2, v86, v87 offset1:1
	v_add_u32_e32 v2, 0x94a0, v110
	s_waitcnt vmcnt(2)
	ds_write2_b32 v2, v88, v89 offset1:1
	v_add_u32_e32 v2, 0x94a8, v110
	ds_write2_b32 v2, v90, v91 offset1:1
	v_add_u32_e32 v2, 0x98c0, v110
	s_waitcnt vmcnt(1)
	ds_write2_b32 v2, v92, v93 offset1:1
	v_add_u32_e32 v2, 0x98c8, v110
	ds_write2_b32 v2, v94, v95 offset1:1
	v_add_u32_e32 v2, 0x9ce0, v110
	s_waitcnt vmcnt(0)
	ds_write2_b32 v2, v96, v97 offset1:1
	v_add_u32_e32 v2, 0x9ce8, v110
	ds_write2_b32 v2, v98, v99 offset1:1
	s_waitcnt lgkmcnt(0)
	v_add_u32_e32 v94, 0x8000, v109
	ds_read2_b32 v[72:73], v94 offset0:33 offset1:41
	ds_read2_b32 v[74:75], v94 offset1:8
	ds_read2_b32 v[76:77], v94 offset0:66 offset1:74
	ds_read2_b32 v[78:79], v94 offset0:99 offset1:107
	ds_read2_b32 v[80:81], v94 offset0:132 offset1:140
	ds_read2_b32 v[82:83], v94 offset0:165 offset1:173
	ds_read2_b32 v[84:85], v94 offset0:198 offset1:206
	ds_read2_b32 v[86:87], v94 offset0:231 offset1:239
	v_add_u32_e32 v2, s27, v106
	v_mad_u64_u32 v[90:91], s[0:1], v2, s22, 0
	s_waitcnt lgkmcnt(6)
	v_cvt_pk_bf16_f32 v68, v74, v72
	v_ashrrev_i32_e32 v72, 31, v2
	v_mov_b32_e32 v2, v91
	s_ashr_i32 s9, s8, 31
	v_mad_u64_u32 v[92:93], s[0:1], v72, s22, v[2:3]
	v_lshl_add_u64 v[88:89], s[8:9], 1, v[104:105]
	v_mov_b32_e32 v91, v92
	s_waitcnt lgkmcnt(4)
	v_cvt_pk_bf16_f32 v69, v76, v78
	s_waitcnt lgkmcnt(2)
	v_cvt_pk_bf16_f32 v70, v80, v82
	s_waitcnt lgkmcnt(0)
	v_cvt_pk_bf16_f32 v71, v84, v86
	v_lshl_add_u64 v[90:91], v[90:91], 1, v[88:89]
	v_add_u32_e32 v2, s27, v1
	global_store_dwordx4 v[90:91], v[68:71], off
	v_ashrrev_i32_e32 v74, 31, v2
	v_mov_b32_e32 v95, v67
	v_cvt_pk_bf16_f32 v68, v75, v73
	v_mad_u64_u32 v[72:73], s[0:1], v2, s22, 0
	v_mov_b32_e32 v2, v73
	v_mad_u64_u32 v[74:75], s[0:1], v74, s22, v[2:3]
	v_mov_b32_e32 v73, v74
	v_cvt_pk_bf16_f32 v69, v77, v79
	v_cvt_pk_bf16_f32 v70, v81, v83
	v_cvt_pk_bf16_f32 v71, v85, v87
	v_lshl_add_u64 v[72:73], v[72:73], 1, v[88:89]
	ds_read2_b32 v[74:75], v94 offset0:16 offset1:24
	ds_read2_b32 v[76:77], v94 offset0:49 offset1:57
	ds_read2_b32 v[78:79], v94 offset0:82 offset1:90
	ds_read2_b32 v[80:81], v94 offset0:115 offset1:123
	ds_read2_b32 v[82:83], v94 offset0:148 offset1:156
	ds_read2_b32 v[84:85], v94 offset0:181 offset1:189
	ds_read2_b32 v[86:87], v94 offset0:214 offset1:222
	ds_read2_b32 v[90:91], v94 offset0:247 offset1:255
	v_add_u32_e32 v2, s27, v107
	global_store_dwordx4 v[72:73], v[68:71], off
	v_mad_u64_u32 v[72:73], s[0:1], v2, s22, 0
	s_waitcnt lgkmcnt(6)
	v_cvt_pk_bf16_f32 v68, v74, v76
	v_ashrrev_i32_e32 v74, 31, v2
	v_mov_b32_e32 v2, v73
	v_mad_u64_u32 v[92:93], s[0:1], v74, s22, v[2:3]
	v_mov_b32_e32 v73, v92
	s_waitcnt lgkmcnt(4)
	v_cvt_pk_bf16_f32 v69, v78, v80
	s_waitcnt lgkmcnt(2)
	v_cvt_pk_bf16_f32 v70, v82, v84
	s_waitcnt lgkmcnt(0)
	v_cvt_pk_bf16_f32 v71, v86, v90
	v_lshl_add_u64 v[72:73], v[72:73], 1, v[88:89]
	v_add_u32_e32 v2, s27, v108
	global_store_dwordx4 v[72:73], v[68:71], off
	v_mad_u64_u32 v[72:73], s[0:1], v2, s22, 0
	v_ashrrev_i32_e32 v74, 31, v2
	v_mov_b32_e32 v2, v73
	v_cvt_pk_bf16_f32 v68, v75, v77
	v_mad_u64_u32 v[74:75], s[0:1], v74, s22, v[2:3]
	v_mov_b32_e32 v73, v74
	v_cvt_pk_bf16_f32 v69, v79, v81
	v_cvt_pk_bf16_f32 v70, v83, v85
	v_cvt_pk_bf16_f32 v71, v87, v91
	v_lshl_add_u64 v[72:73], v[72:73], 1, v[88:89]
	global_store_dwordx4 v[72:73], v[68:71], off
	s_waitcnt lgkmcnt(0)
	v_readlane_b32 s0, v255, 1
	s_lshr_b32 s0, s0, 2
	s_add_i32 s26, s26, s0
	v_mov_b32_e32 v68, v40
	v_mov_b32_e32 v69, v41
	v_mov_b32_e32 v70, v42
	v_mov_b32_e32 v71, v43
	v_mov_b32_e32 v72, v36
	v_mov_b32_e32 v73, v37
	v_mov_b32_e32 v74, v38
	v_mov_b32_e32 v75, v39
	v_mov_b32_e32 v76, v48
	v_mov_b32_e32 v77, v49
	v_mov_b32_e32 v78, v50
	v_mov_b32_e32 v79, v51
	v_mov_b32_e32 v80, v44
	v_mov_b32_e32 v81, v45
	v_mov_b32_e32 v82, v46
	v_mov_b32_e32 v83, v47
	v_mov_b32_e32 v84, v60
	v_mov_b32_e32 v85, v61
	v_mov_b32_e32 v86, v62
	v_mov_b32_e32 v87, v63
	v_mov_b32_e32 v88, v52
	v_mov_b32_e32 v89, v53
	v_mov_b32_e32 v90, v54
	v_mov_b32_e32 v91, v55
	v_mov_b32_e32 v92, v64
	v_mov_b32_e32 v93, v65
	v_mov_b32_e32 v94, v66
	v_mov_b32_e32 v96, v56
	v_mov_b32_e32 v97, v57
	v_mov_b32_e32 v98, v58
	s_cmp_ge_i32 s26, s23
	v_mov_b32_e32 v99, v59
	s_cbranch_scc1 .LBB0_1707
	v_mov_b64_e32 v[58:59], v[30:31]
	v_mov_b64_e32 v[66:67], v[34:35]
	v_mov_b64_e32 v[54:55], v[22:23]
	v_mov_b64_e32 v[62:63], v[26:27]
	v_mov_b64_e32 v[46:47], v[14:15]
	v_mov_b64_e32 v[50:51], v[18:19]
	v_mov_b64_e32 v[38:39], v[6:7]
	v_mov_b64_e32 v[42:43], v[10:11]
	v_mov_b64_e32 v[56:57], v[28:29]
	v_mov_b64_e32 v[64:65], v[32:33]
	v_mov_b64_e32 v[52:53], v[20:21]
	v_mov_b64_e32 v[60:61], v[24:25]
	v_mov_b64_e32 v[44:45], v[12:13]
	v_mov_b64_e32 v[48:49], v[16:17]
	v_mov_b64_e32 v[36:37], v[4:5]
	v_mov_b64_e32 v[40:41], v[8:9]
	s_mov_b32 s27, s12
	s_mov_b32 s8, s11
	s_branch .LBB0_1755
